# baseline (speedup 1.0000x reference)
_Z9k_coarse2PKtS0_PKdS2_Pf:
	s_cmp_lt_u32 s2, 0x100
	s_cbranch_scc1 .Lmy_c2_noprio
	s_setprio 1
.Lmy_c2_noprio:
	s_and_b32 s3, s2, 7
	s_mul_i32 s3, s3, 48
	s_lshr_b32 s2, s2, 3
	s_load_dwordx4 s[4:7], s[0:1], 0x0
	s_add_i32 s3, s3, s2
	s_mul_hi_u32 s10, s3, 0x55555556
	s_mul_i32 s2, s10, 3
	s_sub_i32 s26, s3, s2
	s_mul_hi_u32 s2, s3, 0x2aaaaaab
	s_lshr_b32 s22, s2, 5
	v_cmp_lt_u32_e32 vcc, 63, v0
	v_lshlrev_b32_e32 v1, 3, v0
	s_and_saveexec_b64 s[2:3], vcc
	s_xor_b64 s[2:3], exec, s[2:3]
	s_lshl_b32 s8, s22, 12
	s_not_b32 s9, s26
	v_lshlrev_b32_e32 v74, 3, v0
	v_mov_b32_e32 v72, s9
	v_mov_b32_e32 v83, s8
	s_or_saveexec_b64 s[2:3], s[2:3]
	s_load_dwordx2 s[8:9], s[0:1], 0x10
	s_add_i32 s12, s26, 1
	s_xor_b64 exec, exec, s[2:3]
	s_cbranch_execz .LBB1_4
	s_load_dwordx2 s[14:15], s[0:1], 0x18
	s_lshl_b32 s11, s22, 12
	v_and_or_b32 v23, v1, 56, s11
	v_and_or_b32 v22, v0, 56, 4
	v_or_b32_e32 v24, 4, v23
	s_not_b32 s13, s26
	v_add_lshl_u32 v2, v22, s13, 6
	v_add_u32_e32 v25, s13, v24
	v_or_b32_e32 v4, v25, v2
	v_mov_b32_e32 v5, 0
	s_waitcnt lgkmcnt(0)
	v_lshl_add_u64 v[6:7], v[4:5], 3, s[14:15]
	v_add_u32_e32 v4, v23, v2
	v_mov_b32_e32 v3, v5
	v_lshl_add_u64 v[8:9], v[4:5], 3, s[14:15]
	v_add_u32_e32 v4, s12, v23
	v_lshlrev_b32_e32 v10, 6, v22
	v_lshl_add_u64 v[2:3], v[4:5], 0, v[2:3]
	v_or_b32_e32 v12, v25, v10
	v_mov_b32_e32 v13, v5
	v_lshl_add_u64 v[2:3], v[2:3], 3, s[14:15]
	v_lshl_add_u64 v[12:13], v[12:13], 3, s[14:15]
	global_load_dwordx2 v[14:15], v[6:7], off
	global_load_dwordx2 v[16:17], v[8:9], off offset:32
	global_load_dwordx2 v[18:19], v[2:3], off offset:32
	global_load_dwordx2 v[20:21], v[12:13], off
	v_add_lshl_u32 v8, v22, s12, 6
	v_mov_b32_e32 v11, v5
	v_or_b32_e32 v2, v23, v10
	v_mov_b32_e32 v3, v5
	v_add_u32_e32 v6, v25, v8
	v_add_u32_e32 v8, v24, v8
	v_lshl_add_u64 v[2:3], v[2:3], 3, s[14:15]
	v_lshl_add_u64 v[4:5], v[4:5], 0, v[10:11]
	v_ashrrev_i32_e32 v7, 31, v6
	v_ashrrev_i32_e32 v9, 31, v8
	v_lshl_add_u64 v[4:5], v[4:5], 3, s[14:15]
	v_lshl_add_u64 v[6:7], v[6:7], 3, s[14:15]
	v_lshl_add_u64 v[10:11], v[8:9], 3, s[14:15]
	global_load_dwordx2 v[12:13], v[2:3], off offset:32
	global_load_dwordx2 v[22:23], v[4:5], off offset:32
	global_load_dwordx2 v[24:25], v[6:7], off
	global_load_dwordx2 v[26:27], v[10:11], off
	v_add_u32_e32 v2, s12, v8
	v_ashrrev_i32_e32 v3, 31, v2
	v_lshl_add_u64 v[2:3], v[2:3], 3, s[14:15]
	global_load_dwordx2 v[2:3], v[2:3], off
	s_mov_b32 s14, 0
	s_brev_b32 s15, 8
	v_mov_b32_e32 v6, 0x100
	v_mov_b32_e32 v7, 0xffffff80
	v_mov_b32_e32 v10, 0x260
	s_mov_b32 s16, 0x812dea11
	s_mov_b32 s17, 0x3d719799
	v_mov_b32_e32 v83, s11
	v_mov_b32_e32 v72, s13
	v_mov_b32_e32 v74, v1
	s_waitcnt vmcnt(8)
	v_add_f64 v[4:5], v[14:15], 0
	s_waitcnt vmcnt(7)
	v_add_f64 v[4:5], v[4:5], v[16:17]
	s_waitcnt vmcnt(6)
	v_add_f64 v[4:5], v[4:5], v[18:19]
	s_waitcnt vmcnt(5)
	v_add_f64 v[4:5], v[4:5], v[20:21]
	s_waitcnt vmcnt(4)
	v_add_f64 v[4:5], v[4:5], v[12:13]
	s_waitcnt vmcnt(3)
	v_add_f64 v[4:5], v[4:5], v[22:23]
	s_waitcnt vmcnt(2)
	v_add_f64 v[4:5], v[4:5], v[24:25]
	s_waitcnt vmcnt(1)
	v_add_f64 v[4:5], v[4:5], v[26:27]
	v_lshlrev_b32_e32 v12, 2, v0
	s_waitcnt vmcnt(0)
	v_add_f64 v[2:3], v[4:5], v[2:3]
	v_cmp_gt_f64_e32 vcc, s[14:15], v[2:3]
	s_nop 1
	v_cndmask_b32_e32 v4, 0, v6, vcc
	v_ldexp_f64 v[2:3], v[2:3], v4
	v_rsq_f64_e32 v[4:5], v[2:3]
	v_cndmask_b32_e32 v11, 0, v7, vcc
	v_cmp_class_f64_e32 vcc, v[2:3], v10
	v_mul_f64 v[6:7], v[2:3], v[4:5]
	v_mul_f64 v[4:5], v[4:5], 0.5
	v_fma_f64 v[8:9], -v[4:5], v[6:7], 0.5
	v_fmac_f64_e32 v[6:7], v[6:7], v[8:9]
	v_fmac_f64_e32 v[4:5], v[4:5], v[8:9]
	v_fma_f64 v[8:9], -v[6:7], v[6:7], v[2:3]
	v_fmac_f64_e32 v[6:7], v[8:9], v[4:5]
	v_fma_f64 v[8:9], -v[6:7], v[6:7], v[2:3]
	v_fmac_f64_e32 v[6:7], v[8:9], v[4:5]
	v_ldexp_f64 v[4:5], v[6:7], v11
	v_cndmask_b32_e32 v3, v5, v3, vcc
	v_cndmask_b32_e32 v2, v4, v2, vcc
	v_max_f64 v[2:3], v[2:3], s[16:17]
	v_div_scale_f64 v[4:5], s[14:15], v[2:3], v[2:3], 1.0
	v_rcp_f64_e32 v[6:7], v[4:5]
	v_div_scale_f64 v[8:9], vcc, 1.0, v[2:3], 1.0
	v_fma_f64 v[10:11], -v[4:5], v[6:7], 1.0
	v_fmac_f64_e32 v[6:7], v[6:7], v[10:11]
	v_fma_f64 v[10:11], -v[4:5], v[6:7], 1.0
	v_fmac_f64_e32 v[6:7], v[6:7], v[10:11]
	v_mul_f64 v[10:11], v[8:9], v[6:7]
	v_fma_f64 v[4:5], -v[4:5], v[10:11], v[8:9]
	v_div_fmas_f64 v[4:5], v[4:5], v[6:7], v[10:11]
	v_div_fixup_f64 v[2:3], v[4:5], v[2:3], 1.0
	v_cvt_f32_f64_e32 v2, v[2:3]
	ds_write_b32 v12, v2
